# P7: next unit's token-index gathers issued one K-step earlier so the unit's last step no longer drains the fresh weight loads
# speedup vs baseline: 1.0108x; 1.0033x over previous
; #define MG_STAGE_A(b, rows, k0) do { _Pragma("unroll") for (int h_ = 0; h_ < 2; ++h_) _Pragma("unroll") for (int i_ = 0; i_ < 2; ++i_) if (rows[h_][i_] != 0xffffffffu) \
;         __builtin_amdgcn_global_load_lds((const unsigned*)((const char*)Abase + rows[h_][i_] + (k0) * 2), (PG8_LAS unsigned*)(lds + MG_SA(b, h_) + ldsw + i_ * 8192), 16, 0, 0); } while (0)
; template <class Epi, bool G1> ...
;     ...
;             if (!last) { MG_STAGE_A(buf ^ 1, rowC, (t + 1) * BK); }
;             else if (has_next) { MG_ROWS(nxt, rowC); MG_STAGE_A(buf ^ 1, rowC, 0); }
.LBB0_1094:
	s_or_b64 exec, exec, s[8:9]
	s_and_b64 vcc, exec, s[40:41]
	s_cbranch_vccz .Lg7_skip
	s_ashr_i32 s74, s66, 3
	s_lshl_b32 s75, s74, 2
	s_add_i32 s76, s75, 0x20200
	s_add_i32 s75, s75, 0x20000
	v_mov_b32_e32 v254, s75
	v_mov_b32_e32 v255, s76
	ds_read_b32 v254, v254
	ds_read_b32 v255, v255
	s_lshl_b32 s75, s65, 8
	s_lshl_b32 s74, s74, 14
	v_mov_b32_e32 v250, -1
	v_mov_b32_e32 v251, -1
	v_mov_b32_e32 v252, -1
	v_mov_b32_e32 v253, -1
	s_waitcnt lgkmcnt(0)
	v_add_u32_e32 v255, v255, v254
	v_sub_u32_e32 v254, s74, v254
	v_add_u32_e32 v206, s75, v214
	v_add_u32_e32 v207, s75, v215
	s_bitset1_b32 s75, 7
	v_add_u32_e32 v208, s75, v214
	v_add_u32_e32 v209, s75, v215
	v_cmp_lt_i32_e32 vcc, v206, v255
	s_and_saveexec_b64 s[76:77], vcc
	v_add_u32_e32 v210, v254, v206
	v_ashrrev_i32_e32 v211, 31, v210
	v_lshl_add_u64 v[210:211], v[210:211], 2, s[16:17]
	global_load_dword v250, v[210:211], off
	s_or_b64 exec, exec, s[76:77]
	v_cmp_lt_i32_e32 vcc, v207, v255
	s_and_saveexec_b64 s[76:77], vcc
	v_add_u32_e32 v212, v254, v207
	v_ashrrev_i32_e32 v213, 31, v212
	v_lshl_add_u64 v[212:213], v[212:213], 2, s[16:17]
	global_load_dword v251, v[212:213], off
	s_or_b64 exec, exec, s[76:77]
	v_cmp_lt_i32_e32 vcc, v208, v255
	s_and_saveexec_b64 s[76:77], vcc
	v_add_u32_e32 v226, v254, v208
	v_ashrrev_i32_e32 v227, 31, v226
	v_lshl_add_u64 v[226:227], v[226:227], 2, s[16:17]
	global_load_dword v252, v[226:227], off
	s_or_b64 exec, exec, s[76:77]
	v_cmp_lt_i32_e32 vcc, v209, v255
	s_and_saveexec_b64 s[76:77], vcc
	v_add_u32_e32 v228, v254, v209
	v_ashrrev_i32_e32 v229, 31, v228
	v_lshl_add_u64 v[228:229], v[228:229], 2, s[16:17]
	global_load_dword v253, v[228:229], off
	s_or_b64 exec, exec, s[76:77]
.Lg7_skip:
	s_and_b64 vcc, exec, s[10:11]
	s_cbranch_vccz .LBB0_1120
.LBB0_1095:
	s_and_saveexec_b64 s[6:7], s[20:21]
	s_cbranch_execz .LBB0_1097

; #define MG_STAGE_A(b, rows, k0) do { _Pragma("unroll") for (int h_ = 0; h_ < 2; ++h_) _Pragma("unroll") for (int i_ = 0; i_ < 2; ++i_) if (rows[h_][i_] != 0xffffffffu) \
;         __builtin_amdgcn_global_load_lds((const unsigned*)((const char*)Abase + rows[h_][i_] + (k0) * 2), (PG8_LAS unsigned*)(lds + MG_SA(b, h_) + ldsw + i_ * 8192), 16, 0, 0); } while (0)
; template <class Epi, bool G1> ...
;     ...
;             if (!last) { MG_STAGE_A(buf ^ 1, rowC, (t + 1) * BK); }
;             else if (has_next) { MG_ROWS(nxt, rowC); MG_STAGE_A(buf ^ 1, rowC, 0); }
.LBB0_1119:
	v_lshl_add_u64 v[206:207], s[26:27], 0, v[196:197]
	s_add_i32 s6, s51, s45
	v_lshl_add_u64 v[206:207], v[206:207], 0, s[34:35]
	s_add_i32 m0, s6, 0x6000
	s_nop 0
	global_load_lds_dwordx4 v[206:207], off
	s_branch .LBB0_1094

; #define MG_STAGE_A(b, rows, k0) do { _Pragma("unroll") for (int h_ = 0; h_ < 2; ++h_) _Pragma("unroll") for (int i_ = 0; i_ < 2; ++i_) if (rows[h_][i_] != 0xffffffffu) \
;         __builtin_amdgcn_global_load_lds((const unsigned*)((const char*)Abase + rows[h_][i_] + (k0) * 2), (PG8_LAS unsigned*)(lds + MG_SA(b, h_) + ldsw + i_ * 8192), 16, 0, 0); } while (0)
; template <class Epi, bool G1> ...
;     ...
;             else if (has_next) { MG_ROWS(nxt, rowC); MG_STAGE_A(buf ^ 1, rowC, 0); }
.LBB0_1122:
	v_mov_b32_e32 v194, v250
	v_mov_b32_e32 v192, v251
	v_mov_b32_e32 v198, v252
	v_mov_b32_e32 v193, v253
	v_cmp_ne_u32_e32 vcc, -1, v194
	v_lshlrev_b32_e32 v206, 11, v194
	v_and_b32_e32 v206, 0xfffff000, v206
	v_add_u32_e32 v206, v206, v223
	v_cndmask_b32_e32 v194, v194, v206, vcc
	v_cmp_ne_u32_e32 vcc, -1, v192
	v_lshlrev_b32_e32 v206, 11, v192
	v_and_b32_e32 v206, 0xfffff000, v206
	v_add_u32_e32 v206, v206, v224
	v_cndmask_b32_e32 v192, v192, v206, vcc
	v_cmp_ne_u32_e32 vcc, -1, v198
	v_lshlrev_b32_e32 v206, 11, v198
	v_and_b32_e32 v206, 0xfffff000, v206
	v_add_u32_e32 v206, v206, v223
	v_cndmask_b32_e32 v198, v198, v206, vcc
	v_cmp_ne_u32_e32 vcc, -1, v193
	v_lshlrev_b32_e32 v206, 11, v193
	v_and_b32_e32 v206, 0xfffff000, v206
	v_add_u32_e32 v206, v206, v224
	v_cndmask_b32_e32 v193, v193, v206, vcc
	s_mov_b64 s[14:15], exec
	s_or_b64 exec, exec, s[14:15]
	v_cmp_ne_u32_e32 vcc, -1, v194
	s_and_saveexec_b64 s[14:15], vcc
	s_cbranch_execnz .LBB0_1145
